# baseline (speedup 1.0000x reference)
amdhsa.kernels:
  - .agpr_count:     0
    .args:
      - .offset:         0
        .size:           384
        .value_kind:     by_value
    .group_segment_fixed_size: 5120
    .kernarg_segment_align: 8
    .kernarg_segment_size: 384
    .language:       OpenCL C
    .language_version:
      - 2
      - 0
    .max_flat_workgroup_size: 256
    .name:           _Z6k_prep6WtArgs
    .private_segment_fixed_size: 0
    .sgpr_count:     38
    .sgpr_spill_count: 0
    .symbol:         _Z6k_prep6WtArgs.kd
    .uniform_work_group_size: 1
    .uses_dynamic_stack: false
    .vgpr_count:     29
    .vgpr_spill_count: 0
    .wavefront_size: 64
  - .agpr_count:     0
    .args:
      - .actual_access:  read_only
        .address_space:  global
        .offset:         0
        .size:           8
        .value_kind:     global_buffer
      - .actual_access:  read_only
        .address_space:  global
        .offset:         8
        .size:           8
        .value_kind:     global_buffer
      - .actual_access:  read_only
        .address_space:  global
        .offset:         16
        .size:           8
        .value_kind:     global_buffer
      - .actual_access:  write_only
        .address_space:  global
        .offset:         24
        .size:           8
        .value_kind:     global_buffer
      - .actual_access:  write_only
        .address_space:  global
        .offset:         32
        .size:           8
        .value_kind:     global_buffer
      - .actual_access:  write_only
        .address_space:  global
        .offset:         40
        .size:           8
        .value_kind:     global_buffer
      - .offset:         48
        .size:           4
        .value_kind:     by_value
    .group_segment_fixed_size: 0
    .kernarg_segment_align: 8
    .kernarg_segment_size: 52
    .language:       OpenCL C
    .language_version:
      - 2
      - 0
    .max_flat_workgroup_size: 256
    .name:           _Z4k_lnPKDF16_PKfS2_PfPDF16_Phi
    .private_segment_fixed_size: 0
    .sgpr_count:     18
    .sgpr_spill_count: 0
    .symbol:         _Z4k_lnPKDF16_PKfS2_PfPDF16_Phi.kd
    .uniform_work_group_size: 1
    .uses_dynamic_stack: false
    .vgpr_count:     59
    .vgpr_spill_count: 0
    .wavefront_size: 64
  - .agpr_count:     0
    .args:
      - .offset:         0
        .size:           56
        .value_kind:     by_value
      - .offset:         56
        .size:           72
        .value_kind:     by_value
      - .offset:         128
        .size:           176
        .value_kind:     by_value
      - .address_space:  global
        .offset:         304
        .size:           8
        .value_kind:     global_buffer
      - .offset:         312
        .size:           4
        .value_kind:     hidden_block_count_x
      - .offset:         316
        .size:           4
        .value_kind:     hidden_block_count_y
      - .offset:         320
        .size:           4
        .value_kind:     hidden_block_count_z
      - .offset:         324
        .size:           2
        .value_kind:     hidden_group_size_x
      - .offset:         326
        .size:           2
        .value_kind:     hidden_group_size_y
      - .offset:         328
        .size:           2
        .value_kind:     hidden_group_size_z
      - .offset:         330
        .size:           2
        .value_kind:     hidden_remainder_x
      - .offset:         332
        .size:           2
        .value_kind:     hidden_remainder_y
      - .offset:         334
        .size:           2
        .value_kind:     hidden_remainder_z
      - .offset:         352
        .size:           8
        .value_kind:     hidden_global_offset_x
      - .offset:         360
        .size:           8
        .value_kind:     hidden_global_offset_y
      - .offset:         368
        .size:           8
        .value_kind:     hidden_global_offset_z
      - .offset:         376
        .size:           2
        .value_kind:     hidden_grid_dims
      - .offset:         432
        .size:           4
        .value_kind:     hidden_dynamic_lds_size
    .group_segment_fixed_size: 0
    .kernarg_segment_align: 8
    .kernarg_segment_size: 568
    .language:       OpenCL C
    .language_version:
      - 2
      - 0
    .max_flat_workgroup_size: 512
    .name:           _Z6k_gemmIN3pg84EpiHILi0ELb1EEELb1EEvNS0_4GemmET_6WtTailPj
    .private_segment_fixed_size: 0
    .sgpr_count:     106
    .sgpr_spill_count: 5
    .symbol:         _Z6k_gemmIN3pg84EpiHILi0ELb1EEELb1EEvNS0_4GemmET_6WtTailPj.kd
    .uniform_work_group_size: 1
    .uses_dynamic_stack: false
    .vgpr_count:     240
    .vgpr_spill_count: 0
    .wavefront_size: 64
  - .agpr_count:     0
    .args:
      - .address_space:  global
        .offset:         0
        .size:           8
        .value_kind:     global_buffer
      - .address_space:  global
        .offset:         8
        .size:           8
        .value_kind:     global_buffer
      - .address_space:  global
        .offset:         16
        .size:           8
        .value_kind:     global_buffer
      - .address_space:  global
        .offset:         24
        .size:           8
        .value_kind:     global_buffer
      - .address_space:  global
        .offset:         32
        .size:           8
        .value_kind:     global_buffer
    .group_segment_fixed_size: 0
    .kernarg_segment_align: 8
    .kernarg_segment_size: 40
    .language:       OpenCL C
    .language_version:
      - 2
      - 0
    .max_flat_workgroup_size: 512
    .name:           _Z6k_attnILi1024ELi1024ELi1024ELi1024ELi3072ELi1024ELb1ELb1EEvPKDF16_S1_S1_PKfPDF16_
    .private_segment_fixed_size: 0
    .sgpr_count:     72
    .sgpr_spill_count: 0
    .symbol:         _Z6k_attnILi1024ELi1024ELi1024ELi1024ELi3072ELi1024ELb1ELb1EEvPKDF16_S1_S1_PKfPDF16_.kd
    .uniform_work_group_size: 1
    .uses_dynamic_stack: false
    .vgpr_count:     224
    .vgpr_spill_count: 0
    .wavefront_size: 64
  - .agpr_count:     0
    .args:
      - .address_space:  global
        .offset:         0
        .size:           8
        .value_kind:     global_buffer
      - .address_space:  global
        .offset:         8
        .size:           8
        .value_kind:     global_buffer
      - .offset:         16
        .size:           4
        .value_kind:     by_value
      - .offset:         20
        .size:           4
        .value_kind:     by_value
      - .offset:         24
        .size:           4
        .value_kind:     by_value
      - .offset:         32
        .size:           32
        .value_kind:     by_value
    .group_segment_fixed_size: 0
    .kernarg_segment_align: 8
    .kernarg_segment_size: 64
    .language:       OpenCL C
    .language_version:
      - 2
      - 0
    .max_flat_workgroup_size: 512
    .name:           _ZN2g811k_gemm128f8INS_6EpiResEEEvPKhS3_iiiT_
    .private_segment_fixed_size: 0
    .sgpr_count:     34
    .sgpr_spill_count: 0
    .symbol:         _ZN2g811k_gemm128f8INS_6EpiResEEEvPKhS3_iiiT_.kd
    .uniform_work_group_size: 1
    .uses_dynamic_stack: false
    .vgpr_count:     98
    .vgpr_spill_count: 0
    .wavefront_size: 64
  - .agpr_count:     0
    .args:
      - .address_space:  global
        .offset:         0
        .size:           8
        .value_kind:     global_buffer
      - .address_space:  global
        .offset:         8
        .size:           8
        .value_kind:     global_buffer
      - .offset:         16
        .size:           4
        .value_kind:     by_value
      - .offset:         20
        .size:           4
        .value_kind:     by_value
      - .offset:         24
        .size:           4
        .value_kind:     by_value
      - .offset:         32
        .size:           16
        .value_kind:     by_value
    .group_segment_fixed_size: 0
    .kernarg_segment_align: 8
    .kernarg_segment_size: 48
    .language:       OpenCL C
    .language_version:
      - 2
      - 0
    .max_flat_workgroup_size: 512
    .name:           _ZN2g811k_gemm128f8INS_5EpiQ8EEEvPKhS3_iiiT_
    .private_segment_fixed_size: 0
    .sgpr_count:     30
    .sgpr_spill_count: 0
    .symbol:         _ZN2g811k_gemm128f8INS_5EpiQ8EEEvPKhS3_iiiT_.kd
    .uniform_work_group_size: 1
    .uses_dynamic_stack: false
    .vgpr_count:     240
    .vgpr_spill_count: 0
    .wavefront_size: 64
  - .agpr_count:     0
    .args:
      - .address_space:  global
        .offset:         0
        .size:           8
        .value_kind:     global_buffer
      - .address_space:  global
        .offset:         8
        .size:           8
        .value_kind:     global_buffer
      - .address_space:  global
        .offset:         16
        .size:           8
        .value_kind:     global_buffer
      - .address_space:  global
        .offset:         24
        .size:           8
        .value_kind:     global_buffer
      - .address_space:  global
        .offset:         32
        .size:           8
        .value_kind:     global_buffer
    .group_segment_fixed_size: 0
    .kernarg_segment_align: 8
    .kernarg_segment_size: 40
    .language:       OpenCL C
    .language_version:
      - 2
      - 0
    .max_flat_workgroup_size: 512
    .name:           _Z6k_attnILi1024ELi2048ELi1024ELi1024ELi2048ELi1024ELb1ELb1EEvPKDF16_S1_S1_PKfPDF16_
    .private_segment_fixed_size: 0
    .sgpr_count:     72
    .sgpr_spill_count: 0
    .symbol:         _Z6k_attnILi1024ELi2048ELi1024ELi1024ELi2048ELi1024ELb1ELb1EEvPKDF16_S1_S1_PKfPDF16_.kd
    .uniform_work_group_size: 1
    .uses_dynamic_stack: false
    .vgpr_count:     224
    .vgpr_spill_count: 0
    .wavefront_size: 64
  - .agpr_count:     0
    .args:
      - .offset:         0
        .size:           56
        .value_kind:     by_value
      - .offset:         56
        .size:           72
        .value_kind:     by_value
      - .offset:         128
        .size:           176
        .value_kind:     by_value
      - .address_space:  global
        .offset:         304
        .size:           8
        .value_kind:     global_buffer
      - .offset:         312
        .size:           4
        .value_kind:     hidden_block_count_x
      - .offset:         316
        .size:           4
        .value_kind:     hidden_block_count_y
      - .offset:         320
        .size:           4
        .value_kind:     hidden_block_count_z
      - .offset:         324
        .size:           2
        .value_kind:     hidden_group_size_x
      - .offset:         326
        .size:           2
        .value_kind:     hidden_group_size_y
      - .offset:         328
        .size:           2
        .value_kind:     hidden_group_size_z
      - .offset:         330
        .size:           2
        .value_kind:     hidden_remainder_x
      - .offset:         332
        .size:           2
        .value_kind:     hidden_remainder_y
      - .offset:         334
        .size:           2
        .value_kind:     hidden_remainder_z
      - .offset:         352
        .size:           8
        .value_kind:     hidden_global_offset_x
      - .offset:         360
        .size:           8
        .value_kind:     hidden_global_offset_y
      - .offset:         368
        .size:           8
        .value_kind:     hidden_global_offset_z
      - .offset:         376
        .size:           2
        .value_kind:     hidden_grid_dims
      - .offset:         432
        .size:           4
        .value_kind:     hidden_dynamic_lds_size
    .group_segment_fixed_size: 0
    .kernarg_segment_align: 8
    .kernarg_segment_size: 568
    .language:       OpenCL C
    .language_version:
      - 2
      - 0
    .max_flat_workgroup_size: 512
    .name:           _Z6k_gemmIN3pg84EpiHILi1ELb0EEELb0EEvNS0_4GemmET_6WtTailPj
    .private_segment_fixed_size: 0
    .sgpr_count:     85
    .sgpr_spill_count: 0
    .symbol:         _Z6k_gemmIN3pg84EpiHILi1ELb0EEELb0EEvNS0_4GemmET_6WtTailPj.kd
    .uniform_work_group_size: 1
    .uses_dynamic_stack: false
    .vgpr_count:     242
    .vgpr_spill_count: 0
    .wavefront_size: 64
  - .agpr_count:     0
    .args:
      - .address_space:  global
        .offset:         0
        .size:           8
        .value_kind:     global_buffer
      - .address_space:  global
        .offset:         8
        .size:           8
        .value_kind:     global_buffer
      - .offset:         16
        .size:           4
        .value_kind:     by_value
      - .offset:         20
        .size:           4
        .value_kind:     by_value
      - .offset:         24
        .size:           4
        .value_kind:     by_value
      - .offset:         32
        .size:           32
        .value_kind:     by_value
    .group_segment_fixed_size: 0
    .kernarg_segment_align: 8
    .kernarg_segment_size: 64
    .language:       OpenCL C
    .language_version:
      - 2
      - 0
    .max_flat_workgroup_size: 512
    .name:           _ZN4g1289k_gemm128INS_8EpiRes16EEEvPKDF16_S3_iiiT_
    .private_segment_fixed_size: 0
    .sgpr_count:     35
    .sgpr_spill_count: 0
    .symbol:         _ZN4g1289k_gemm128INS_8EpiRes16EEEvPKDF16_S3_iiiT_.kd
    .uniform_work_group_size: 1
    .uses_dynamic_stack: false
    .vgpr_count:     112
    .vgpr_spill_count: 0
    .wavefront_size: 64
